# attention unit epilogue: 64 two-byte global stores per lane replaced by an LDS transpose through the wave-private stash words and 8 dwordx4 stores (plus SrcC init change)
# speedup vs baseline: 1.0035x; 1.0035x over previous
; __device__ __forceinline__ float bf_lo(unsigned w) { return __uint_as_float(w << 16); }
; __device__ __forceinline__ float bf_hi(unsigned w) { return __uint_as_float(w & 0xffff0000u); }
;     __device__ __forceinline__ float* lam() const { return (float*)(ws + WS_LAM); }
; __device__ __forceinline__ void attn_unit(bf16_t* __restrict__ proj, LAS char* lds, int qrow0, int b, int h, int NT, float lam, float post, const float* __restrict__ gsub) {
;     ...
; #pragma unroll
;     for (int d = 0; d < 4; ++d)
; #pragma unroll
;         for (int r = 0; r < 16; r += 2) {
;             const unsigned w = stash[(d * 8 + (r >> 1)) * NTHR + tid];
;             const float a0 = bf_lo(w) - lam * o[d][r], a1 = bf_hi(w) - lam * o[d][r + 1];
;             o[d][r] = a0; o[d][r + 1] = a1; ss[r] += a0 * a0; ss[r + 1] += a1 * a1;
;         }
.LBB0_340:
	v_mov_b32_e32 v106, v0
	v_mov_b32_e32 v6, v98
	v_lshl_add_u32 v2, v106, 2, 0
	v_add_u32_e32 v107, 0x12800, v2
	ds_read2st64_b32 v[4:5], v107 offset0:64 offset1:72
	ds_read2st64_b32 v[12:13], v107 offset1:8
	ds_read2st64_b32 v[26:27], v107 offset0:16 offset1:24
	ds_read2st64_b32 v[40:41], v107 offset0:32 offset1:40
	ds_read2st64_b32 v[50:51], v107 offset0:48 offset1:56
	ds_read2st64_b32 v[30:31], v107 offset0:80 offset1:88
	s_waitcnt lgkmcnt(5)
	v_lshlrev_b32_e32 v3, 16, v4
	s_waitcnt lgkmcnt(4)
	v_lshlrev_b32_e32 v2, 16, v12
	v_mov_b32_e32 v7, v104
	v_pk_fma_f32 v[2:3], v[168:169], v[6:7], v[2:3] neg_lo:[1,0,0] neg_hi:[1,0,0]
	v_and_b32_e32 v7, 0xffff0000, v4
	v_lshlrev_b32_e32 v9, 16, v5
	v_lshlrev_b32_e32 v8, 16, v13
	v_mov_b32_e32 v14, v92
	v_mov_b32_e32 v15, v102
	v_and_b32_e32 v5, 0xffff0000, v5
	v_and_b32_e32 v4, 0xffff0000, v13
	v_mov_b32_e32 v102, v93
	v_and_b32_e32 v6, 0xffff0000, v12
	v_pk_fma_f32 v[8:9], v[168:169], v[14:15], v[8:9] neg_lo:[1,0,0] neg_hi:[1,0,0]
	v_pk_fma_f32 v[14:15], v[168:169], v[102:103], v[4:5] neg_lo:[1,0,0] neg_hi:[1,0,0]
	s_waitcnt lgkmcnt(0)
	v_lshlrev_b32_e32 v5, 16, v30
	v_lshlrev_b32_e32 v4, 16, v26
	v_mov_b32_e32 v12, v88
	v_mov_b32_e32 v13, v100
	v_pk_fma_f32 v[16:17], v[168:169], v[12:13], v[4:5] neg_lo:[1,0,0] neg_hi:[1,0,0]
	v_and_b32_e32 v5, 0xffff0000, v30
	v_and_b32_e32 v4, 0xffff0000, v26
	v_mov_b32_e32 v100, v89
	v_pk_fma_f32 v[20:21], v[168:169], v[100:101], v[4:5] neg_lo:[1,0,0] neg_hi:[1,0,0]
	v_lshlrev_b32_e32 v5, 16, v31
	v_lshlrev_b32_e32 v4, 16, v27
	v_mov_b32_e32 v12, v84
	v_mov_b32_e32 v13, v96
	v_pk_fma_f32 v[22:23], v[168:169], v[12:13], v[4:5] neg_lo:[1,0,0] neg_hi:[1,0,0]
	ds_read2st64_b32 v[12:13], v107 offset0:96 offset1:104
	v_and_b32_e32 v5, 0xffff0000, v31
	v_and_b32_e32 v4, 0xffff0000, v27
	v_mov_b32_e32 v96, v85
	v_pk_fma_f32 v[26:27], v[168:169], v[96:97], v[4:5] neg_lo:[1,0,0] neg_hi:[1,0,0]
	s_waitcnt lgkmcnt(0)
	v_lshlrev_b32_e32 v5, 16, v12
	v_lshlrev_b32_e32 v4, 16, v40
	v_mov_b32_e32 v30, v80
	v_mov_b32_e32 v31, v94
	v_pk_fma_f32 v[30:31], v[168:169], v[30:31], v[4:5] neg_lo:[1,0,0] neg_hi:[1,0,0]
	v_and_b32_e32 v5, 0xffff0000, v12
	v_and_b32_e32 v4, 0xffff0000, v40
	v_mov_b32_e32 v94, v81
	v_pk_fma_f32 v[32:33], v[168:169], v[94:95], v[4:5] neg_lo:[1,0,0] neg_hi:[1,0,0]
	v_lshlrev_b32_e32 v5, 16, v13
	v_lshlrev_b32_e32 v4, 16, v41
	v_mov_b32_e32 v36, v76
	v_mov_b32_e32 v37, v90
	v_pk_fma_f32 v[36:37], v[168:169], v[36:37], v[4:5] neg_lo:[1,0,0] neg_hi:[1,0,0]
	v_and_b32_e32 v5, 0xffff0000, v13
	ds_read2st64_b32 v[12:13], v107 offset0:112 offset1:120
	v_and_b32_e32 v4, 0xffff0000, v41
	v_mov_b32_e32 v90, v77
	v_pk_fma_f32 v[40:41], v[168:169], v[90:91], v[4:5] neg_lo:[1,0,0] neg_hi:[1,0,0]
	v_lshlrev_b32_e32 v4, 16, v50
	s_waitcnt lgkmcnt(0)
	v_lshlrev_b32_e32 v5, 16, v12
	v_mov_b32_e32 v42, v72
	v_mov_b32_e32 v43, v86
	v_pk_fma_f32 v[42:43], v[168:169], v[42:43], v[4:5] neg_lo:[1,0,0] neg_hi:[1,0,0]
	v_and_b32_e32 v5, 0xffff0000, v12
	v_and_b32_e32 v4, 0xffff0000, v50
	v_mov_b32_e32 v86, v73
	v_pk_fma_f32 v[44:45], v[168:169], v[86:87], v[4:5] neg_lo:[1,0,0] neg_hi:[1,0,0]
	v_lshlrev_b32_e32 v5, 16, v13
	v_lshlrev_b32_e32 v4, 16, v51
	v_mov_b32_e32 v48, v70
	v_mov_b32_e32 v49, v82
	v_pk_fma_f32 v[48:49], v[168:169], v[48:49], v[4:5] neg_lo:[1,0,0] neg_hi:[1,0,0]
	v_and_b32_e32 v5, 0xffff0000, v13
	v_and_b32_e32 v4, 0xffff0000, v51
	v_mov_b32_e32 v82, v71
	v_pk_fma_f32 v[52:53], v[168:169], v[82:83], v[4:5] neg_lo:[1,0,0] neg_hi:[1,0,0]
	ds_read2st64_b32 v[50:51], v107 offset0:192 offset1:200
	ds_read2st64_b32 v[82:83], v107 offset0:128 offset1:136
	ds_read2st64_b32 v[108:109], v107 offset0:144 offset1:152
	ds_read2st64_b32 v[110:111], v107 offset0:160 offset1:168
	ds_read2st64_b32 v[112:113], v107 offset0:176 offset1:184
	s_waitcnt lgkmcnt(4)
	v_lshlrev_b32_e32 v5, 16, v50
	s_waitcnt lgkmcnt(3)
	v_lshlrev_b32_e32 v4, 16, v82
	v_mov_b32_e32 v12, v18
	v_mov_b32_e32 v13, v10
	v_pk_mul_f32 v[56:57], v[2:3], v[2:3]
	v_pk_fma_f32 v[4:5], v[168:169], v[12:13], v[4:5] neg_lo:[1,0,0] neg_hi:[1,0,0]
	v_add_f32_e32 v10, v56, v57
	v_pk_mul_f32 v[12:13], v[4:5], v[4:5]
	v_mov_b32_e32 v104, v99
	v_add_f32_e32 v10, v10, v12
	v_pk_fma_f32 v[6:7], v[168:169], v[104:105], v[6:7] neg_lo:[1,0,0] neg_hi:[1,0,0]
	v_add_f32_e32 v114, v10, v13
	v_and_b32_e32 v13, 0xffff0000, v50
	v_and_b32_e32 v12, 0xffff0000, v82
	v_mov_b32_e32 v10, v19
	v_pk_mul_f32 v[98:99], v[6:7], v[6:7]
	v_pk_fma_f32 v[10:11], v[168:169], v[10:11], v[12:13] neg_lo:[1,0,0] neg_hi:[1,0,0]
	v_add_f32_e32 v18, v98, v99
	v_pk_mul_f32 v[12:13], v[10:11], v[10:11]
	v_mov_b32_e32 v19, v54
	v_add_f32_e32 v12, v18, v12
	v_add_f32_e32 v82, v12, v13
	v_lshlrev_b32_e32 v13, 16, v51
	v_lshlrev_b32_e32 v12, 16, v83
	v_mov_b32_e32 v18, v24
	v_pk_mul_f32 v[104:105], v[8:9], v[8:9]
	v_pk_fma_f32 v[12:13], v[168:169], v[18:19], v[12:13] neg_lo:[1,0,0] neg_hi:[1,0,0]
	v_add_f32_e32 v24, v104, v105
	v_pk_mul_f32 v[18:19], v[12:13], v[12:13]
	v_mov_b32_e32 v54, v25
	v_add_f32_e32 v18, v24, v18
	v_add_f32_e32 v104, v18, v19
	v_and_b32_e32 v19, 0xffff0000, v51
	ds_read2st64_b32 v[50:51], v107 offset0:208 offset1:216
	v_and_b32_e32 v18, 0xffff0000, v83
	v_pk_mul_f32 v[92:93], v[14:15], v[14:15]
	v_pk_fma_f32 v[18:19], v[168:169], v[54:55], v[18:19] neg_lo:[1,0,0] neg_hi:[1,0,0]
	v_add_f32_e32 v54, v92, v93
	v_pk_mul_f32 v[24:25], v[18:19], v[18:19]
	v_mov_b32_e32 v55, v34
	v_add_f32_e32 v24, v54, v24
	v_add_f32_e32 v83, v24, v25
	s_waitcnt lgkmcnt(0)
; __device__ __forceinline__ float bf_lo(unsigned w) { return __uint_as_float(w << 16); }
; __device__ __forceinline__ float bf_hi(unsigned w) { return __uint_as_float(w & 0xffff0000u); }
;     __device__ __forceinline__ float* lam() const { return (float*)(ws + WS_LAM); }
; __device__ __forceinline__ void attn_unit(bf16_t* __restrict__ proj, LAS char* lds, int qrow0, int b, int h, int NT, float lam, float post, const float* __restrict__ gsub) {
;     ...
; #pragma unroll
;     for (int d = 0; d < 4; ++d)
; #pragma unroll
;         for (int r = 0; r < 16; r += 2) {
;             const unsigned w = stash[(d * 8 + (r >> 1)) * NTHR + tid];
;             const float a0 = bf_lo(w) - lam * o[d][r], a1 = bf_hi(w) - lam * o[d][r + 1];
;             o[d][r] = a0; o[d][r + 1] = a1; ss[r] += a0 * a0; ss[r + 1] += a1 * a1;
;         }
; #pragma unroll
;     for (int r = 0; r < 16; ++r) {
;         const float v = half32_sum(ss[r]);
;         ss[r] = rsqrtf(v * (1.f / 128.f) + EPS) * post;
;     }
	v_lshlrev_b32_e32 v25, 16, v50
	v_lshlrev_b32_e32 v24, 16, v108
	v_mov_b32_e32 v54, v28
	v_pk_mul_f32 v[102:103], v[16:17], v[16:17]
	v_pk_fma_f32 v[24:25], v[168:169], v[54:55], v[24:25] neg_lo:[1,0,0] neg_hi:[1,0,0]
	v_add_f32_e32 v28, v102, v103
	v_pk_mul_f32 v[54:55], v[24:25], v[24:25]
	v_mov_b32_e32 v34, v29
	v_add_f32_e32 v28, v28, v54
	v_add_f32_e32 v92, v28, v55
	v_and_b32_e32 v55, 0xffff0000, v50
	v_and_b32_e32 v54, 0xffff0000, v108
	v_pk_mul_f32 v[88:89], v[20:21], v[20:21]
	v_pk_fma_f32 v[28:29], v[168:169], v[34:35], v[54:55] neg_lo:[1,0,0] neg_hi:[1,0,0]
	v_add_f32_e32 v50, v88, v89
	v_pk_mul_f32 v[34:35], v[28:29], v[28:29]
	v_mov_b32_e32 v54, v46
	v_add_f32_e32 v34, v50, v34
	v_add_f32_e32 v88, v34, v35
	v_lshlrev_b32_e32 v35, 16, v51
	v_lshlrev_b32_e32 v34, 16, v109
	v_mov_b32_e32 v55, v38
	v_pk_mul_f32 v[100:101], v[22:23], v[22:23]
	v_pk_fma_f32 v[34:35], v[168:169], v[54:55], v[34:35] neg_lo:[1,0,0] neg_hi:[1,0,0]
	v_add_f32_e32 v38, v100, v101
	v_pk_mul_f32 v[54:55], v[34:35], v[34:35]
	ds_read2st64_b32 v[56:57], v107 offset0:224 offset1:232
	v_add_f32_e32 v38, v38, v54
	v_add_f32_e32 v89, v38, v55
	v_and_b32_e32 v51, 0xffff0000, v51
	v_and_b32_e32 v50, 0xffff0000, v109
	v_mov_b32_e32 v38, v47
	v_pk_mul_f32 v[84:85], v[26:27], v[26:27]
	v_pk_fma_f32 v[38:39], v[168:169], v[38:39], v[50:51] neg_lo:[1,0,0] neg_hi:[1,0,0]
	v_add_f32_e32 v50, v84, v85
	v_pk_mul_f32 v[46:47], v[38:39], v[38:39]
	v_mov_b32_e32 v51, v58
	v_add_f32_e32 v46, v50, v46
	v_add_f32_e32 v84, v46, v47
	s_waitcnt lgkmcnt(0)
	v_lshlrev_b32_e32 v47, 16, v56
	v_lshlrev_b32_e32 v46, 16, v110
	v_mov_b32_e32 v50, v78
	v_pk_mul_f32 v[96:97], v[30:31], v[30:31]
	v_pk_fma_f32 v[46:47], v[168:169], v[50:51], v[46:47] neg_lo:[1,0,0] neg_hi:[1,0,0]
	v_add_f32_e32 v54, v96, v97
	v_pk_mul_f32 v[50:51], v[46:47], v[46:47]
	v_mov_b32_e32 v58, v79
	v_add_f32_e32 v50, v54, v50
	v_add_f32_e32 v78, v50, v51
	v_and_b32_e32 v51, 0xffff0000, v56
	v_and_b32_e32 v50, 0xffff0000, v110
	v_pk_mul_f32 v[80:81], v[32:33], v[32:33]
	v_pk_fma_f32 v[50:51], v[168:169], v[58:59], v[50:51] neg_lo:[1,0,0] neg_hi:[1,0,0]
	v_add_f32_e32 v56, v80, v81
	v_pk_mul_f32 v[54:55], v[50:51], v[50:51]
	v_mov_b32_e32 v58, v74
	v_add_f32_e32 v54, v56, v54
	v_add_f32_e32 v79, v54, v55
	v_lshlrev_b32_e32 v55, 16, v57
	v_lshlrev_b32_e32 v54, 16, v111
	v_mov_b32_e32 v59, v60
	v_pk_mul_f32 v[94:95], v[36:37], v[36:37]
	v_pk_fma_f32 v[54:55], v[168:169], v[58:59], v[54:55] neg_lo:[1,0,0] neg_hi:[1,0,0]
	v_add_f32_e32 v56, v94, v95
	v_pk_mul_f32 v[58:59], v[54:55], v[54:55]
	v_mov_b32_e32 v60, v75
	v_add_f32_e32 v56, v56, v58
	ds_read2st64_b32 v[74:75], v107 offset0:240 offset1:248
	v_add_f32_e32 v80, v56, v59
	v_and_b32_e32 v57, 0xffff0000, v57
	v_and_b32_e32 v56, 0xffff0000, v111
	v_pk_mul_f32 v[76:77], v[40:41], v[40:41]
	v_pk_fma_f32 v[56:57], v[168:169], v[60:61], v[56:57] neg_lo:[1,0,0] neg_hi:[1,0,0]
	v_add_f32_e32 v60, v76, v77
	v_pk_mul_f32 v[58:59], v[56:57], v[56:57]
	v_mov_b32_e32 v61, v62
	v_add_f32_e32 v58, v60, v58
	v_add_f32_e32 v76, v58, v59
	s_waitcnt lgkmcnt(0)
	v_lshlrev_b32_e32 v59, 16, v74
	v_lshlrev_b32_e32 v58, 16, v112
	v_mov_b32_e32 v60, v68
	v_pk_mul_f32 v[90:91], v[42:43], v[42:43]
	v_pk_fma_f32 v[58:59], v[168:169], v[60:61], v[58:59] neg_lo:[1,0,0] neg_hi:[1,0,0]
	v_add_f32_e32 v62, v90, v91
	v_pk_mul_f32 v[60:61], v[58:59], v[58:59]
	v_pk_mul_f32 v[72:73], v[44:45], v[44:45]
	v_add_f32_e32 v60, v62, v60
	v_add_f32_e32 v77, v60, v61
	v_and_b32_e32 v61, 0xffff0000, v74
	v_and_b32_e32 v60, 0xffff0000, v112
	v_mov_b32_e32 v62, v69
	v_pk_fma_f32 v[60:61], v[168:169], v[62:63], v[60:61] neg_lo:[1,0,0] neg_hi:[1,0,0]
	v_add_f32_e32 v68, v72, v73
	v_pk_mul_f32 v[62:63], v[60:61], v[60:61]
	v_mov_b32_e32 v69, v64
	v_add_f32_e32 v62, v68, v62
	v_add_f32_e32 v72, v62, v63
	v_lshlrev_b32_e32 v63, 16, v75
	v_lshlrev_b32_e32 v62, 16, v113
	v_mov_b32_e32 v68, v66
	v_pk_mul_f32 v[86:87], v[48:49], v[48:49]
	v_pk_fma_f32 v[62:63], v[168:169], v[68:69], v[62:63] neg_lo:[1,0,0] neg_hi:[1,0,0]
	v_add_f32_e32 v64, v86, v87
	v_pk_mul_f32 v[68:69], v[62:63], v[62:63]
	v_pk_mul_f32 v[70:71], v[52:53], v[52:53]
	v_add_f32_e32 v64, v64, v68
	v_add_f32_e32 v73, v64, v69
	v_and_b32_e32 v69, 0xffff0000, v75
	v_and_b32_e32 v68, 0xffff0000, v113
	v_mov_b32_e32 v64, v67
	v_pk_fma_f32 v[64:65], v[168:169], v[64:65], v[68:69] neg_lo:[1,0,0] neg_hi:[1,0,0]
	v_add_f32_e32 v68, v70, v71
	v_pk_mul_f32 v[66:67], v[64:65], v[64:65]
	s_mov_b32 s0, 0x358637bd
	v_add_f32_e32 v66, v68, v66
	v_add_f32_e32 v74, v66, v67
	v_and_b32_e32 v75, 31, v106
	v_add_f32_dpp v66, v114, v114 quad_perm:[1,0,3,2] row_mask:0xf bank_mask:0xf bound_ctrl:1
	v_lshlrev_b32_e32 v109, 2, v75
	global_load_dword v112, v109, s[46:47]
	v_add_f32_dpp v66, v66, v66 quad_perm:[2,3,0,1] row_mask:0xf bank_mask:0xf bound_ctrl:1
	s_lshl_b32 s76, s31, 1
	v_lshlrev_b32_e32 v146, 1, v75
	v_add_f32_dpp v66, v66, v66 row_half_mirror row_mask:0xf bank_mask:0xf bound_ctrl:1
	s_add_i32 s2, s23, 1
	v_readlane_b32 s8, v254, 62
	v_add_f32_dpp v67, v66, v66 row_mirror row_mask:0xf bank_mask:0xf bound_ctrl:1
	v_add_f32_dpp v66, v82, v82 quad_perm:[1,0,3,2] row_mask:0xf bank_mask:0xf bound_ctrl:1
	v_mov_b32_e32 v69, v67
	s_nop 1
	v_permlane16_swap_b32_e32 v67, v69
	v_add_f32_dpp v66, v66, v66 quad_perm:[2,3,0,1] row_mask:0xf bank_mask:0xf bound_ctrl:1
	v_readlane_b32 s9, v254, 63
	s_nop 0
	v_add_f32_dpp v66, v66, v66 row_half_mirror row_mask:0xf bank_mask:0xf bound_ctrl:1
	s_nop 1
	v_add_f32_dpp v66, v66, v66 row_mirror row_mask:0xf bank_mask:0xf bound_ctrl:1
	v_mov_b32_e32 v68, v66
	s_nop 1
	v_permlane16_swap_b32_e32 v66, v68
	v_pk_add_f32 v[68:69], v[66:67], v[68:69]
	v_mov_b64_e32 v[66:67], s[0:1]
	s_brev_b32 s0, 60
	v_pk_fma_f32 v[68:69], v[68:69], s[0:1], v[66:67] op_sel_hi:[1,0,0]
	s_nop 0
	v_mul_f32_e32 v70, 0x4b800000, v69
	v_cmp_gt_f32_e32 vcc, s3, v69
	v_cmp_gt_f32_e64 s[40:41], s3, v68
	s_nop 0
	v_cndmask_b32_e32 v69, v69, v70, vcc
	v_rsq_f32_e32 v69, v69
	v_mul_f32_e32 v70, 0x4b800000, v68
	v_cndmask_b32_e64 v68, v68, v70, s[40:41]
	v_rsq_f32_e32 v68, v68
	v_mul_f32_e32 v70, 0x45800000, v69
	v_cndmask_b32_e32 v69, v69, v70, vcc
	v_mul_f32_e32 v99, v1, v69
	v_mul_f32_e32 v69, 0x45800000, v68
	v_cndmask_b32_e64 v68, v68, v69, s[40:41]
	v_mul_f32_e32 v98, v1, v68
	v_mul_f32_e32 v2, v2, v99
	v_add_f32_dpp v68, v104, v104 quad_perm:[1,0,3,2] row_mask:0xf bank_mask:0xf bound_ctrl:1
	v_mul_f32_e32 v4, v4, v99
	s_waitcnt vmcnt(0)
; __device__ __forceinline__ void attn_unit(bf16_t* __restrict__ proj, LAS char* lds, int qrow0, int b, int h, int NT, float lam, float post, const float* __restrict__ gsub) {
;     ...
; #pragma unroll
;     for (int r = 0; r < 16; ++r) {
;         const float v = half32_sum(ss[r]);
;         ss[r] = rsqrtf(v * (1.f / 128.f) + EPS) * post;
;     }
	v_mul_f32_e32 v2, v2, v112
	v_add_f32_dpp v68, v68, v68 quad_perm:[2,3,0,1] row_mask:0xf bank_mask:0xf bound_ctrl:1
	v_cvt_pk_bf16_f32 v2, v2, v147
	s_nop 1
	v_add_f32_dpp v68, v68, v68 row_half_mirror row_mask:0xf bank_mask:0xf bound_ctrl:1
	s_nop 1
	v_add_f32_dpp v69, v68, v68 row_mirror row_mask:0xf bank_mask:0xf bound_ctrl:1
	v_add_f32_dpp v68, v83, v83 quad_perm:[1,0,3,2] row_mask:0xf bank_mask:0xf bound_ctrl:1
	v_mov_b32_e32 v71, v69
	s_nop 1
	v_permlane16_swap_b32_e32 v69, v71
	v_add_f32_dpp v68, v68, v68 quad_perm:[2,3,0,1] row_mask:0xf bank_mask:0xf bound_ctrl:1
	s_nop 1
	v_add_f32_dpp v68, v68, v68 row_half_mirror row_mask:0xf bank_mask:0xf bound_ctrl:1
	s_nop 1
	v_add_f32_dpp v68, v68, v68 row_mirror row_mask:0xf bank_mask:0xf bound_ctrl:1
	v_mov_b32_e32 v70, v68
	s_nop 1
	v_permlane16_swap_b32_e32 v68, v70
	v_pk_add_f32 v[68:69], v[68:69], v[70:71]
	s_nop 0
	v_pk_fma_f32 v[68:69], v[68:69], s[0:1], v[66:67] op_sel_hi:[1,0,0]
	s_nop 0
	v_mul_f32_e32 v70, 0x4b800000, v69
	v_cmp_gt_f32_e32 vcc, s3, v69
	v_cmp_gt_f32_e64 s[40:41], s3, v68
	s_nop 0
	v_cndmask_b32_e32 v69, v69, v70, vcc
	v_rsq_f32_e32 v69, v69
	v_mul_f32_e32 v70, 0x4b800000, v68
	v_cndmask_b32_e64 v68, v68, v70, s[40:41]
	v_rsq_f32_e32 v68, v68
	v_mul_f32_e32 v70, 0x45800000, v69
	v_cndmask_b32_e32 v69, v69, v70, vcc
	v_mul_f32_e32 v101, v1, v69
	v_mul_f32_e32 v69, 0x45800000, v68
	v_cndmask_b32_e64 v68, v68, v69, s[40:41]
	v_mul_f32_e32 v100, v1, v68
	s_nop 0
	v_add_f32_dpp v68, v92, v92 quad_perm:[1,0,3,2] row_mask:0xf bank_mask:0xf bound_ctrl:1
	s_nop 1
	v_add_f32_dpp v68, v68, v68 quad_perm:[2,3,0,1] row_mask:0xf bank_mask:0xf bound_ctrl:1
	s_nop 1
	v_add_f32_dpp v68, v68, v68 row_half_mirror row_mask:0xf bank_mask:0xf bound_ctrl:1
	s_nop 1
	v_add_f32_dpp v69, v68, v68 row_mirror row_mask:0xf bank_mask:0xf bound_ctrl:1
	v_add_f32_dpp v68, v88, v88 quad_perm:[1,0,3,2] row_mask:0xf bank_mask:0xf bound_ctrl:1
	v_mov_b32_e32 v71, v69
	s_nop 1
	v_permlane16_swap_b32_e32 v69, v71
	v_add_f32_dpp v68, v68, v68 quad_perm:[2,3,0,1] row_mask:0xf bank_mask:0xf bound_ctrl:1
	s_nop 1
	v_add_f32_dpp v68, v68, v68 row_half_mirror row_mask:0xf bank_mask:0xf bound_ctrl:1
	s_nop 1
	v_add_f32_dpp v68, v68, v68 row_mirror row_mask:0xf bank_mask:0xf bound_ctrl:1
	v_mov_b32_e32 v70, v68
	s_nop 1
	v_permlane16_swap_b32_e32 v68, v70
	v_pk_add_f32 v[68:69], v[68:69], v[70:71]
	s_nop 0
	v_pk_fma_f32 v[68:69], v[68:69], s[0:1], v[66:67] op_sel_hi:[1,0,0]
	s_nop 0
	v_mul_f32_e32 v70, 0x4b800000, v69
	v_cmp_gt_f32_e32 vcc, s3, v69
	v_cmp_gt_f32_e64 s[40:41], s3, v68
	s_nop 0
	v_cndmask_b32_e32 v69, v69, v70, vcc
	v_rsq_f32_e32 v69, v69
	v_mul_f32_e32 v70, 0x4b800000, v68
	v_cndmask_b32_e64 v68, v68, v70, s[40:41]
	v_rsq_f32_e32 v68, v68
	v_mul_f32_e32 v70, 0x45800000, v69
	v_cndmask_b32_e32 v69, v69, v70, vcc
	v_mul_f32_e32 v103, v1, v69
	v_mul_f32_e32 v69, 0x45800000, v68
	v_cndmask_b32_e64 v68, v68, v69, s[40:41]
	v_mul_f32_e32 v102, v1, v68
	s_nop 0
	v_add_f32_dpp v68, v89, v89 quad_perm:[1,0,3,2] row_mask:0xf bank_mask:0xf bound_ctrl:1
	s_nop 1
	v_add_f32_dpp v68, v68, v68 quad_perm:[2,3,0,1] row_mask:0xf bank_mask:0xf bound_ctrl:1
	s_nop 1
	v_add_f32_dpp v68, v68, v68 row_half_mirror row_mask:0xf bank_mask:0xf bound_ctrl:1
	s_nop 1
	v_add_f32_dpp v69, v68, v68 row_mirror row_mask:0xf bank_mask:0xf bound_ctrl:1
	v_add_f32_dpp v68, v84, v84 quad_perm:[1,0,3,2] row_mask:0xf bank_mask:0xf bound_ctrl:1
	v_mov_b32_e32 v71, v69
	s_nop 1
	v_permlane16_swap_b32_e32 v69, v71
	v_add_f32_dpp v68, v68, v68 quad_perm:[2,3,0,1] row_mask:0xf bank_mask:0xf bound_ctrl:1
	s_nop 1
	v_add_f32_dpp v68, v68, v68 row_half_mirror row_mask:0xf bank_mask:0xf bound_ctrl:1
	s_nop 1
	v_add_f32_dpp v68, v68, v68 row_mirror row_mask:0xf bank_mask:0xf bound_ctrl:1
	v_mov_b32_e32 v70, v68
	s_nop 1
	v_permlane16_swap_b32_e32 v68, v70
	v_pk_add_f32 v[68:69], v[68:69], v[70:71]
	s_nop 0
	v_pk_fma_f32 v[68:69], v[68:69], s[0:1], v[66:67] op_sel_hi:[1,0,0]
	s_nop 0
	v_mul_f32_e32 v70, 0x4b800000, v69
	v_cmp_gt_f32_e32 vcc, s3, v69
	v_cmp_gt_f32_e64 s[40:41], s3, v68
	s_nop 0
	v_cndmask_b32_e32 v69, v69, v70, vcc
	v_rsq_f32_e32 v69, v69
	v_mul_f32_e32 v70, 0x4b800000, v68
	v_cndmask_b32_e64 v68, v68, v70, s[40:41]
	v_rsq_f32_e32 v68, v68
	v_mul_f32_e32 v70, 0x45800000, v69
	v_cndmask_b32_e32 v69, v69, v70, vcc
	v_mul_f32_e32 v105, v1, v69
	v_mul_f32_e32 v69, 0x45800000, v68
	v_cndmask_b32_e64 v68, v68, v69, s[40:41]
	v_mul_f32_e32 v104, v1, v68
	s_nop 0
	v_add_f32_dpp v68, v78, v78 quad_perm:[1,0,3,2] row_mask:0xf bank_mask:0xf bound_ctrl:1
	s_nop 1
	v_add_f32_dpp v68, v68, v68 quad_perm:[2,3,0,1] row_mask:0xf bank_mask:0xf bound_ctrl:1
	s_nop 1
	v_add_f32_dpp v68, v68, v68 row_half_mirror row_mask:0xf bank_mask:0xf bound_ctrl:1
	s_nop 1
	v_add_f32_dpp v69, v68, v68 row_mirror row_mask:0xf bank_mask:0xf bound_ctrl:1
	v_add_f32_dpp v68, v79, v79 quad_perm:[1,0,3,2] row_mask:0xf bank_mask:0xf bound_ctrl:1
	v_mov_b32_e32 v71, v69
	s_nop 1
	v_permlane16_swap_b32_e32 v69, v71
	v_add_f32_dpp v68, v68, v68 quad_perm:[2,3,0,1] row_mask:0xf bank_mask:0xf bound_ctrl:1
	s_nop 1
	v_add_f32_dpp v68, v68, v68 row_half_mirror row_mask:0xf bank_mask:0xf bound_ctrl:1
	s_nop 1
	v_add_f32_dpp v68, v68, v68 row_mirror row_mask:0xf bank_mask:0xf bound_ctrl:1
	v_mov_b32_e32 v70, v68
	s_nop 1
	v_permlane16_swap_b32_e32 v68, v70
	v_pk_add_f32 v[68:69], v[68:69], v[70:71]
	s_nop 0
	v_pk_fma_f32 v[68:69], v[68:69], s[0:1], v[66:67] op_sel_hi:[1,0,0]
	s_nop 0
	v_mul_f32_e32 v70, 0x4b800000, v69
	v_cmp_gt_f32_e32 vcc, s3, v69
	v_cmp_gt_f32_e64 s[40:41], s3, v68
	s_nop 0
	v_cndmask_b32_e32 v69, v69, v70, vcc
	v_rsq_f32_e32 v69, v69
; __device__ __forceinline__ bf16_t f2bf(float f) { return (bf16_t)(cvt_pk_bf16(f, 0.f) & 0xffffu); }
;     __device__ __forceinline__ bf16_t* proj() const { return (bf16_t*)(ws + WS_PROJ); }
; __device__ __forceinline__ int crow(int r, int hi) { return (r & 3) + 8 * (r >> 2) + 4 * hi; }
; __device__ __forceinline__ void attn_unit(bf16_t* __restrict__ proj, LAS char* lds, int qrow0, int b, int h, int NT, float lam, float post, const float* __restrict__ gsub) {
;     ...
; #pragma unroll
;     for (int r = 0; r < 16; ++r) {
;         const float v = half32_sum(ss[r]);
;         ss[r] = rsqrtf(v * (1.f / 128.f) + EPS) * post;
;     }
;     bf16_t* Ow = proj + (size_t)(qrow0 + wid * 32) * INW + C_Q + h * 128;
; #pragma unroll
;     for (int d = 0; d < 4; ++d) { const float g = gsub[d * 32 + r32];
; #pragma unroll
;         for (int r = 0; r < 16; ++r) Ow[(size_t)crow(r, hi) * INW + d * 32 + r32] = f2bf(o[d][r] * ss[r] * g); }
	v_mul_f32_e32 v70, 0x4b800000, v68
	v_cndmask_b32_e64 v68, v68, v70, s[40:41]
	v_rsq_f32_e32 v68, v68
	v_mul_f32_e32 v70, 0x45800000, v69
	v_cndmask_b32_e32 v69, v69, v70, vcc
	v_mul_f32_e32 v108, v1, v69
	v_mul_f32_e32 v69, 0x45800000, v68
	v_cndmask_b32_e64 v68, v68, v69, s[40:41]
	v_mul_f32_e32 v107, v1, v68
	s_nop 0
	v_add_f32_dpp v68, v80, v80 quad_perm:[1,0,3,2] row_mask:0xf bank_mask:0xf bound_ctrl:1
	s_nop 1
	v_add_f32_dpp v68, v68, v68 quad_perm:[2,3,0,1] row_mask:0xf bank_mask:0xf bound_ctrl:1
	s_nop 1
	v_add_f32_dpp v68, v68, v68 row_half_mirror row_mask:0xf bank_mask:0xf bound_ctrl:1
	s_nop 1
	v_add_f32_dpp v69, v68, v68 row_mirror row_mask:0xf bank_mask:0xf bound_ctrl:1
	v_add_f32_dpp v68, v76, v76 quad_perm:[1,0,3,2] row_mask:0xf bank_mask:0xf bound_ctrl:1
	v_mov_b32_e32 v71, v69
	s_nop 1
	v_permlane16_swap_b32_e32 v69, v71
	v_add_f32_dpp v68, v68, v68 quad_perm:[2,3,0,1] row_mask:0xf bank_mask:0xf bound_ctrl:1
	s_nop 1
	v_add_f32_dpp v68, v68, v68 row_half_mirror row_mask:0xf bank_mask:0xf bound_ctrl:1
	s_nop 1
	v_add_f32_dpp v68, v68, v68 row_mirror row_mask:0xf bank_mask:0xf bound_ctrl:1
	v_mov_b32_e32 v70, v68
	s_nop 1
	v_permlane16_swap_b32_e32 v68, v70
	v_pk_add_f32 v[68:69], v[68:69], v[70:71]
	s_nop 0
	v_pk_fma_f32 v[68:69], v[68:69], s[0:1], v[66:67] op_sel_hi:[1,0,0]
	s_nop 0
	v_mul_f32_e32 v70, 0x4b800000, v69
	v_cmp_gt_f32_e32 vcc, s3, v69
	v_cmp_gt_f32_e64 s[40:41], s3, v68
	s_nop 0
	v_cndmask_b32_e32 v69, v69, v70, vcc
	v_rsq_f32_e32 v69, v69
	v_mul_f32_e32 v70, 0x4b800000, v68
	v_cndmask_b32_e64 v68, v68, v70, s[40:41]
	v_rsq_f32_e32 v68, v68
	v_mul_f32_e32 v70, 0x45800000, v69
	v_cndmask_b32_e32 v69, v69, v70, vcc
	v_mul_f32_e32 v113, v1, v69
	v_mul_f32_e32 v69, 0x45800000, v68
	v_cndmask_b32_e64 v68, v68, v69, s[40:41]
	v_mul_f32_e32 v114, v1, v68
	s_nop 0
	v_add_f32_dpp v68, v77, v77 quad_perm:[1,0,3,2] row_mask:0xf bank_mask:0xf bound_ctrl:1
	s_nop 1
	v_add_f32_dpp v68, v68, v68 quad_perm:[2,3,0,1] row_mask:0xf bank_mask:0xf bound_ctrl:1
	s_nop 1
	v_add_f32_dpp v68, v68, v68 row_half_mirror row_mask:0xf bank_mask:0xf bound_ctrl:1
	s_nop 1
	v_add_f32_dpp v69, v68, v68 row_mirror row_mask:0xf bank_mask:0xf bound_ctrl:1
	v_add_f32_dpp v68, v72, v72 quad_perm:[1,0,3,2] row_mask:0xf bank_mask:0xf bound_ctrl:1
	v_mov_b32_e32 v71, v69
	s_nop 1
	v_permlane16_swap_b32_e32 v69, v71
	v_add_f32_dpp v68, v68, v68 quad_perm:[2,3,0,1] row_mask:0xf bank_mask:0xf bound_ctrl:1
	s_nop 1
	v_add_f32_dpp v68, v68, v68 row_half_mirror row_mask:0xf bank_mask:0xf bound_ctrl:1
	s_nop 1
	v_add_f32_dpp v68, v68, v68 row_mirror row_mask:0xf bank_mask:0xf bound_ctrl:1
	v_mov_b32_e32 v70, v68
	s_nop 1
	v_permlane16_swap_b32_e32 v68, v70
	v_pk_add_f32 v[68:69], v[68:69], v[70:71]
	s_nop 0
	v_pk_fma_f32 v[68:69], v[68:69], s[0:1], v[66:67] op_sel_hi:[1,0,0]
	s_nop 0
	v_mul_f32_e32 v70, 0x4b800000, v69
	v_cmp_gt_f32_e32 vcc, s3, v69
	v_cmp_gt_f32_e64 s[40:41], s3, v68
	s_nop 0
	v_cndmask_b32_e32 v69, v69, v70, vcc
	v_rsq_f32_e32 v69, v69
	v_mul_f32_e32 v70, 0x4b800000, v68
	v_cndmask_b32_e64 v68, v68, v70, s[40:41]
	v_rsq_f32_e32 v68, v68
	v_mul_f32_e32 v70, 0x45800000, v69
	v_cndmask_b32_e32 v69, v69, v70, vcc
	v_mul_f32_e32 v115, v1, v69
	v_mul_f32_e32 v69, 0x45800000, v68
	v_cndmask_b32_e64 v68, v68, v69, s[40:41]
	v_mul_f32_e32 v116, v1, v68
	s_nop 0
	v_add_f32_dpp v68, v73, v73 quad_perm:[1,0,3,2] row_mask:0xf bank_mask:0xf bound_ctrl:1
	s_nop 1
	v_add_f32_dpp v68, v68, v68 quad_perm:[2,3,0,1] row_mask:0xf bank_mask:0xf bound_ctrl:1
	s_nop 1
	v_add_f32_dpp v68, v68, v68 row_half_mirror row_mask:0xf bank_mask:0xf bound_ctrl:1
	s_nop 1
	v_add_f32_dpp v69, v68, v68 row_mirror row_mask:0xf bank_mask:0xf bound_ctrl:1
	v_add_f32_dpp v68, v74, v74 quad_perm:[1,0,3,2] row_mask:0xf bank_mask:0xf bound_ctrl:1
	v_mov_b32_e32 v71, v69
	s_nop 1
	v_permlane16_swap_b32_e32 v69, v71
	v_add_f32_dpp v68, v68, v68 quad_perm:[2,3,0,1] row_mask:0xf bank_mask:0xf bound_ctrl:1
	s_nop 1
	v_add_f32_dpp v68, v68, v68 row_half_mirror row_mask:0xf bank_mask:0xf bound_ctrl:1
	s_nop 1
	v_add_f32_dpp v68, v68, v68 row_mirror row_mask:0xf bank_mask:0xf bound_ctrl:1
	v_mov_b32_e32 v70, v68
	s_nop 1
	v_permlane16_swap_b32_e32 v68, v70
	v_pk_add_f32 v[68:69], v[68:69], v[70:71]
	v_mov_b32_e32 v71, v147
	v_pk_fma_f32 v[66:67], v[68:69], s[0:1], v[66:67] op_sel_hi:[1,0,0]
	s_mov_b64 s[0:1], 0xc0
	v_mul_f32_e32 v68, 0x4b800000, v67
	v_cmp_gt_f32_e32 vcc, s3, v67
	v_cmp_gt_f32_e64 s[40:41], s3, v66
	s_nop 0
	v_cndmask_b32_e32 v67, v67, v68, vcc
	v_rsq_f32_e32 v67, v67
	v_mul_f32_e32 v68, 0x4b800000, v66
	v_cndmask_b32_e64 v66, v66, v68, s[40:41]
	v_rsq_f32_e32 v66, v66
	v_mul_f32_e32 v68, 0x45800000, v67
	v_cndmask_b32_e32 v67, v67, v68, vcc
	v_mul_f32_e32 v117, v1, v67
	v_mul_f32_e32 v67, 0x45800000, v66
	v_cndmask_b32_e64 v66, v66, v67, s[40:41]
	v_mul_f32_e32 v118, v1, v66
	v_ashrrev_i32_e32 v66, 1, v106
	v_and_b32_e32 v66, 0xffffffe0, v66
	v_add_u32_e32 v66, s30, v66
	v_ashrrev_i32_e32 v67, 31, v66
	v_lshlrev_b64 v[66:67], 13, v[66:67]
	v_lshl_add_u64 v[66:67], s[48:49], 0, v[66:67]
	v_lshl_add_u64 v[66:67], v[66:67], 0, s[76:77]
	v_lshlrev_b32_e32 v68, 10, v106
	v_lshl_add_u64 v[66:67], v[66:67], 0, v[146:147]
	v_and_b32_e32 v146, 0x8000, v68
	v_lshl_add_u64 v[68:69], v[66:67], 0, v[146:147]
	v_and_b32_e32 v162, 31, v0
	v_lshlrev_b32_e32 v162, 1, v162
	v_lshrrev_b32_e32 v163, 6, v0
	v_lshl_add_u32 v162, v163, 8, v162
	v_bfe_u32 v163, v0, 5, 1
	v_lshl_add_u32 v162, v163, 13, v162
	v_add_u32_e32 v162, 0x12800, v162
	ds_write_b16 v162, v2 offset:0
	v_mul_f32_e32 v2, v6, v98
	v_mul_f32_e32 v2, v2, v112
	v_or_b32_e32 v70, 0x2000, v146
	v_cvt_pk_bf16_f32 v2, v2, v147
; __device__ __forceinline__ bf16_t f2bf(float f) { return (bf16_t)(cvt_pk_bf16(f, 0.f) & 0xffffu); }
;     __device__ __forceinline__ bf16_t* proj() const { return (bf16_t*)(ws + WS_PROJ); }
; __device__ __forceinline__ int crow(int r, int hi) { return (r & 3) + 8 * (r >> 2) + 4 * hi; }
; __device__ __forceinline__ void attn_unit(bf16_t* __restrict__ proj, LAS char* lds, int qrow0, int b, int h, int NT, float lam, float post, const float* __restrict__ gsub) {
;     ...
;     bf16_t* Ow = proj + (size_t)(qrow0 + wid * 32) * INW + C_Q + h * 128;
; #pragma unroll
;     for (int d = 0; d < 4; ++d) { const float g = gsub[d * 32 + r32];
; #pragma unroll
;         for (int r = 0; r < 16; ++r) Ow[(size_t)crow(r, hi) * INW + d * 32 + r32] = f2bf(o[d][r] * ss[r] * g); }
	v_lshl_add_u64 v[72:73], v[66:67], 0, v[70:71]
	ds_write_b16 v162, v2 offset:2048
	v_mul_f32_e32 v2, v8, v101
	v_mul_f32_e32 v2, v2, v112
	v_or_b32_e32 v72, 0x4000, v146
	v_mov_b32_e32 v73, v147
	v_cvt_pk_bf16_f32 v2, v2, v147
	v_lshl_add_u64 v[74:75], v[66:67], 0, v[72:73]
	ds_write_b16 v162, v2 offset:4096
	v_mul_f32_e32 v2, v14, v100
	v_mul_f32_e32 v2, v2, v112
	v_or_b32_e32 v74, 0x6000, v146
	v_mov_b32_e32 v75, v147
	v_cvt_pk_bf16_f32 v2, v2, v147
	v_lshl_add_u64 v[76:77], v[66:67], 0, v[74:75]
	ds_write_b16 v162, v2 offset:6144
	v_mul_f32_e32 v2, v16, v103
	v_mul_f32_e32 v2, v2, v112
	v_or_b32_e32 v76, 0x10000, v146
	v_mov_b32_e32 v77, v147
	v_cvt_pk_bf16_f32 v2, v2, v147
	v_lshl_add_u64 v[78:79], v[66:67], 0, v[76:77]
	ds_write_b16 v162, v2 offset:16384
	v_mul_f32_e32 v2, v20, v102
	v_mul_f32_e32 v2, v2, v112
	v_or_b32_e32 v78, 0x12000, v146
	v_mov_b32_e32 v79, v147
	v_cvt_pk_bf16_f32 v2, v2, v147
	v_lshl_add_u64 v[80:81], v[66:67], 0, v[78:79]
	ds_write_b16 v162, v2 offset:18432
	v_mul_f32_e32 v2, v22, v105
	v_mul_f32_e32 v2, v2, v112
	v_or_b32_e32 v80, 0x14000, v146
	v_mov_b32_e32 v81, v147
	v_cvt_pk_bf16_f32 v2, v2, v147
	v_lshl_add_u64 v[82:83], v[66:67], 0, v[80:81]
	ds_write_b16 v162, v2 offset:20480
	v_mul_f32_e32 v2, v26, v104
	v_mul_f32_e32 v2, v2, v112
	v_or_b32_e32 v82, 0x16000, v146
	v_mov_b32_e32 v83, v147
	v_cvt_pk_bf16_f32 v2, v2, v147
	v_lshl_add_u64 v[84:85], v[66:67], 0, v[82:83]
	ds_write_b16 v162, v2 offset:22528
	v_mul_f32_e32 v2, v30, v108
	v_mul_f32_e32 v2, v2, v112
	v_or_b32_e32 v84, 0x20000, v146
	v_mov_b32_e32 v85, v147
	v_cvt_pk_bf16_f32 v2, v2, v147
	v_lshl_add_u64 v[86:87], v[66:67], 0, v[84:85]
	ds_write_b16 v162, v2 offset:32768
	v_mul_f32_e32 v2, v32, v107
	v_mul_f32_e32 v2, v2, v112
	v_or_b32_e32 v86, 0x22000, v146
	v_mov_b32_e32 v87, v147
	v_cvt_pk_bf16_f32 v2, v2, v147
	v_lshl_add_u64 v[88:89], v[66:67], 0, v[86:87]
	ds_write_b16 v162, v2 offset:34816
	v_mul_f32_e32 v2, v36, v113
	v_mul_f32_e32 v2, v2, v112
	v_or_b32_e32 v88, 0x24000, v146
	v_mov_b32_e32 v89, v147
	v_cvt_pk_bf16_f32 v2, v2, v147
	v_lshl_add_u64 v[90:91], v[66:67], 0, v[88:89]
	ds_write_b16 v162, v2 offset:36864
	v_mul_f32_e32 v2, v40, v114
	v_mul_f32_e32 v2, v2, v112
	v_or_b32_e32 v90, 0x26000, v146
	v_mov_b32_e32 v91, v147
	v_cvt_pk_bf16_f32 v2, v2, v147
	v_lshl_add_u64 v[92:93], v[66:67], 0, v[90:91]
	ds_write_b16 v162, v2 offset:38912
	v_mul_f32_e32 v2, v42, v115
	v_mul_f32_e32 v2, v2, v112
	v_or_b32_e32 v92, 0x30000, v146
	v_mov_b32_e32 v93, v147
	v_cvt_pk_bf16_f32 v2, v2, v147
	v_lshl_add_u64 v[94:95], v[66:67], 0, v[92:93]
	ds_write_b16 v162, v2 offset:49152
	v_mul_f32_e32 v2, v44, v116
	v_mul_f32_e32 v2, v112, v2
	v_or_b32_e32 v94, 0x32000, v146
	v_mov_b32_e32 v95, v147
	v_cvt_pk_bf16_f32 v2, v2, v147
	v_lshl_add_u64 v[96:97], v[66:67], 0, v[94:95]
	ds_write_b16 v162, v2 offset:51200
	v_mul_f32_e32 v2, v48, v117
	v_mul_f32_e32 v2, v112, v2
	v_or_b32_e32 v96, 0x34000, v146
	v_mov_b32_e32 v97, v147
	v_cvt_pk_bf16_f32 v2, v2, v147
	v_lshl_add_u64 v[110:111], v[66:67], 0, v[96:97]
	ds_write_b16 v162, v2 offset:53248
	v_mul_f32_e32 v2, v52, v118
	v_mul_f32_e32 v2, v112, v2
	v_cvt_pk_bf16_f32 v2, v2, v147
	global_load_dword v6, v109, s[46:47] offset:128
	v_or_b32_e32 v146, 0x36000, v146
	v_lshl_add_u64 v[110:111], v[66:67], 0, v[146:147]
	ds_write_b16 v162, v2 offset:55296
	v_mul_f32_e32 v2, v3, v99
	v_lshl_add_u64 v[110:111], v[66:67], 0, 64
	s_waitcnt vmcnt(0)
	v_mul_f32_e32 v2, v2, v6
	v_cvt_pk_bf16_f32 v2, v2, v147
	ds_write_b16 v162, v2 offset:64
	v_mul_f32_e32 v2, v7, v98
	v_mul_f32_e32 v2, v2, v6
	v_cvt_pk_bf16_f32 v7, v2, v147
	v_lshl_add_u64 v[2:3], v[110:111], 0, v[70:71]
	ds_write_b16 v162, v7 offset:2112
	v_mul_f32_e32 v2, v9, v101
	v_mul_f32_e32 v2, v2, v6
	v_cvt_pk_bf16_f32 v7, v2, v147
	v_lshl_add_u64 v[2:3], v[110:111], 0, v[72:73]
	ds_write_b16 v162, v7 offset:4160
	v_mul_f32_e32 v2, v15, v100
	v_mul_f32_e32 v2, v2, v6
	v_cvt_pk_bf16_f32 v7, v2, v147
	v_lshl_add_u64 v[2:3], v[110:111], 0, v[74:75]
	ds_write_b16 v162, v7 offset:6208
	v_mul_f32_e32 v2, v17, v103
	v_mul_f32_e32 v2, v2, v6
	v_cvt_pk_bf16_f32 v7, v2, v147
	v_lshl_add_u64 v[2:3], v[110:111], 0, v[76:77]
	ds_write_b16 v162, v7 offset:16448
	v_mul_f32_e32 v2, v21, v102
	v_mul_f32_e32 v2, v2, v6
	v_cvt_pk_bf16_f32 v7, v2, v147
	v_lshl_add_u64 v[2:3], v[110:111], 0, v[78:79]
	ds_write_b16 v162, v7 offset:18496
	v_mul_f32_e32 v2, v23, v105
	v_mul_f32_e32 v2, v2, v6
	v_cvt_pk_bf16_f32 v7, v2, v147
	v_lshl_add_u64 v[2:3], v[110:111], 0, v[80:81]
	ds_write_b16 v162, v7 offset:20544
	v_mul_f32_e32 v2, v27, v104
	v_mul_f32_e32 v2, v2, v6
	v_cvt_pk_bf16_f32 v7, v2, v147
	v_lshl_add_u64 v[2:3], v[110:111], 0, v[82:83]
	ds_write_b16 v162, v7 offset:22592
	v_mul_f32_e32 v2, v31, v108
	v_mul_f32_e32 v2, v2, v6
	v_cvt_pk_bf16_f32 v7, v2, v147
	v_lshl_add_u64 v[2:3], v[110:111], 0, v[84:85]
	ds_write_b16 v162, v7 offset:32832
	v_mul_f32_e32 v2, v33, v107
	v_mul_f32_e32 v2, v2, v6
	v_cvt_pk_bf16_f32 v7, v2, v147
	v_lshl_add_u64 v[2:3], v[110:111], 0, v[86:87]
	ds_write_b16 v162, v7 offset:34880
	v_mul_f32_e32 v2, v37, v113
	v_mul_f32_e32 v2, v2, v6
	v_cvt_pk_bf16_f32 v7, v2, v147
	v_lshl_add_u64 v[2:3], v[110:111], 0, v[88:89]
	ds_write_b16 v162, v7 offset:36928
	v_mul_f32_e32 v2, v41, v114
	v_mul_f32_e32 v2, v2, v6
	v_cvt_pk_bf16_f32 v7, v2, v147
	v_lshl_add_u64 v[2:3], v[110:111], 0, v[90:91]
	ds_write_b16 v162, v7 offset:38976
	v_mul_f32_e32 v2, v43, v115
	v_mul_f32_e32 v2, v2, v6
	v_cvt_pk_bf16_f32 v7, v2, v147
	v_lshl_add_u64 v[2:3], v[110:111], 0, v[92:93]
	ds_write_b16 v162, v7 offset:49216
	v_mul_f32_e32 v2, v45, v116
	v_mul_f32_e32 v2, v2, v6
	v_cvt_pk_bf16_f32 v7, v2, v147
	v_lshl_add_u64 v[2:3], v[110:111], 0, v[94:95]
	ds_write_b16 v162, v7 offset:51264
	v_mul_f32_e32 v2, v49, v117
	v_mul_f32_e32 v2, v2, v6
	v_cvt_pk_bf16_f32 v7, v2, v147
	v_lshl_add_u64 v[2:3], v[110:111], 0, v[96:97]
	ds_write_b16 v162, v7 offset:53312
	v_mul_f32_e32 v2, v53, v118
	v_mul_f32_e32 v2, v2, v6
	v_cvt_pk_bf16_f32 v6, v2, v147
	global_load_dword v8, v109, s[46:47] offset:256
	v_lshl_add_u64 v[2:3], v[110:111], 0, v[146:147]
	ds_write_b16 v162, v6 offset:55360
	v_lshl_add_u64 v[2:3], v[66:67], 0, s[34:35]
	v_lshl_add_u64 v[6:7], v[2:3], 0, v[70:71]
	s_waitcnt vmcnt(0)
; __device__ __forceinline__ bf16_t f2bf(float f) { return (bf16_t)(cvt_pk_bf16(f, 0.f) & 0xffffu); }
;     __device__ __forceinline__ bf16_t* proj() const { return (bf16_t*)(ws + WS_PROJ); }
; __device__ __forceinline__ int crow(int r, int hi) { return (r & 3) + 8 * (r >> 2) + 4 * hi; }
; __device__ __forceinline__ void attn_unit(bf16_t* __restrict__ proj, LAS char* lds, int qrow0, int b, int h, int NT, float lam, float post, const float* __restrict__ gsub) {
;     ...
;     bf16_t* Ow = proj + (size_t)(qrow0 + wid * 32) * INW + C_Q + h * 128;
; #pragma unroll
;     for (int d = 0; d < 4; ++d) { const float g = gsub[d * 32 + r32];
; #pragma unroll
;         for (int r = 0; r < 16; ++r) Ow[(size_t)crow(r, hi) * INW + d * 32 + r32] = f2bf(o[d][r] * ss[r] * g); }
; __device__ __forceinline__ void phase_attn(const Frame& F, const Params& P, int l) {
;     ...
;     for (int i = 0;; ++i) {
;         int u = i * F.nwg + F.wg;
;         if (F.nwg == 256 && i < 4) u = ((i * 8 + (F.wg & 7)) << 5) + (F.wg >> 3);
;         if (u >= nun) break;
	v_mul_f32_e32 v4, v4, v8
	v_cvt_pk_bf16_f32 v4, v4, v147
	ds_write_b16 v162, v4 offset:128
	v_mul_f32_e32 v4, v10, v98
	v_mul_f32_e32 v4, v4, v8
	v_cvt_pk_bf16_f32 v4, v4, v147
	ds_write_b16 v162, v4 offset:2176
	v_mul_f32_e32 v4, v12, v101
	v_mul_f32_e32 v4, v4, v8
	v_cvt_pk_bf16_f32 v4, v4, v147
	v_lshl_add_u64 v[6:7], v[2:3], 0, v[72:73]
	ds_write_b16 v162, v4 offset:4224
	v_mul_f32_e32 v4, v18, v100
	v_mul_f32_e32 v4, v4, v8
	v_cvt_pk_bf16_f32 v4, v4, v147
	v_lshl_add_u64 v[6:7], v[2:3], 0, v[74:75]
	ds_write_b16 v162, v4 offset:6272
	v_mul_f32_e32 v4, v24, v103
	v_mul_f32_e32 v4, v4, v8
	v_cvt_pk_bf16_f32 v4, v4, v147
	v_lshl_add_u64 v[6:7], v[2:3], 0, v[76:77]
	ds_write_b16 v162, v4 offset:16512
	v_mul_f32_e32 v4, v28, v102
	v_mul_f32_e32 v4, v4, v8
	v_cvt_pk_bf16_f32 v4, v4, v147
	v_lshl_add_u64 v[6:7], v[2:3], 0, v[78:79]
	ds_write_b16 v162, v4 offset:18560
	v_mul_f32_e32 v4, v34, v105
	v_mul_f32_e32 v4, v4, v8
	v_cvt_pk_bf16_f32 v4, v4, v147
	v_lshl_add_u64 v[6:7], v[2:3], 0, v[80:81]
	ds_write_b16 v162, v4 offset:20608
	v_mul_f32_e32 v4, v38, v104
	v_mul_f32_e32 v4, v4, v8
	v_cvt_pk_bf16_f32 v4, v4, v147
	v_lshl_add_u64 v[6:7], v[2:3], 0, v[82:83]
	ds_write_b16 v162, v4 offset:22656
	v_mul_f32_e32 v4, v46, v108
	v_mul_f32_e32 v4, v4, v8
	v_cvt_pk_bf16_f32 v4, v4, v147
	v_lshl_add_u64 v[6:7], v[2:3], 0, v[84:85]
	ds_write_b16 v162, v4 offset:32896
	v_mul_f32_e32 v4, v50, v107
	v_mul_f32_e32 v4, v4, v8
	v_cvt_pk_bf16_f32 v4, v4, v147
	v_lshl_add_u64 v[6:7], v[2:3], 0, v[86:87]
	ds_write_b16 v162, v4 offset:34944
	v_mul_f32_e32 v4, v54, v113
	v_mul_f32_e32 v4, v4, v8
	v_cvt_pk_bf16_f32 v4, v4, v147
	v_lshl_add_u64 v[6:7], v[2:3], 0, v[88:89]
	ds_write_b16 v162, v4 offset:36992
	v_mul_f32_e32 v4, v56, v114
	v_mul_f32_e32 v4, v4, v8
	v_cvt_pk_bf16_f32 v4, v4, v147
	v_lshl_add_u64 v[6:7], v[2:3], 0, v[90:91]
	ds_write_b16 v162, v4 offset:39040
	v_mul_f32_e32 v4, v58, v115
	v_mul_f32_e32 v4, v4, v8
	v_cvt_pk_bf16_f32 v4, v4, v147
	v_lshl_add_u64 v[6:7], v[2:3], 0, v[92:93]
	ds_write_b16 v162, v4 offset:49280
	v_mul_f32_e32 v4, v60, v116
	v_mul_f32_e32 v4, v4, v8
	v_cvt_pk_bf16_f32 v4, v4, v147
	v_lshl_add_u64 v[6:7], v[2:3], 0, v[94:95]
	ds_write_b16 v162, v4 offset:51328
	v_mul_f32_e32 v4, v62, v117
	v_mul_f32_e32 v4, v4, v8
	v_cvt_pk_bf16_f32 v4, v4, v147
	v_lshl_add_u64 v[6:7], v[2:3], 0, v[96:97]
	ds_write_b16 v162, v4 offset:53376
	v_mul_f32_e32 v4, v64, v118
	v_mul_f32_e32 v4, v4, v8
	v_cvt_pk_bf16_f32 v4, v4, v147
	global_load_dword v6, v109, s[46:47] offset:384
	v_lshl_add_u64 v[2:3], v[2:3], 0, v[146:147]
	ds_write_b16 v162, v4 offset:55424
	v_mul_f32_e32 v4, v5, v99
	v_lshl_add_u64 v[2:3], v[66:67], 0, s[0:1]
	s_mul_i32 s0, s2, s96
	s_add_i32 s7, s0, s8
	s_cmp_lt_u32 s23, 3
	v_readlane_b32 s8, v252, 61
	s_cselect_b64 s[0:1], -1, 0
	v_readlane_b32 s9, v252, 62
	s_and_b64 s[0:1], s[8:9], s[0:1]
	s_lshl_b32 s8, s2, 8
	v_readlane_b32 s9, v252, 63
	s_add_i32 s8, s9, s8
	s_and_b64 s[0:1], s[0:1], exec
	s_cselect_b32 s0, s8, s7
	s_cmp_lt_i32 s0, s22
	s_mov_b32 s23, s2
	s_waitcnt vmcnt(0)
; __device__ __forceinline__ bf16_t f2bf(float f) { return (bf16_t)(cvt_pk_bf16(f, 0.f) & 0xffffu); }
;     __device__ __forceinline__ bf16_t* proj() const { return (bf16_t*)(ws + WS_PROJ); }
; __device__ __forceinline__ int crow(int r, int hi) { return (r & 3) + 8 * (r >> 2) + 4 * hi; }
; __device__ __forceinline__ void attn_unit(bf16_t* __restrict__ proj, LAS char* lds, int qrow0, int b, int h, int NT, float lam, float post, const float* __restrict__ gsub) {
;     ...
;     bf16_t* Ow = proj + (size_t)(qrow0 + wid * 32) * INW + C_Q + h * 128;
; #pragma unroll
;     for (int d = 0; d < 4; ++d) { const float g = gsub[d * 32 + r32];
; #pragma unroll
;         for (int r = 0; r < 16; ++r) Ow[(size_t)crow(r, hi) * INW + d * 32 + r32] = f2bf(o[d][r] * ss[r] * g); }
; __device__ __forceinline__ void phase_attn(const Frame& F, const Params& P, int l) {
;     ...
;     for (int i = 0;; ++i) {
;         int u = i * F.nwg + F.wg;
;         if (F.nwg == 256 && i < 4) u = ((i * 8 + (F.wg & 7)) << 5) + (F.wg >> 3);
;         if (u >= nun) break;
	v_mul_f32_e32 v4, v4, v6
	v_cvt_pk_bf16_f32 v4, v4, v147
	ds_write_b16 v162, v4 offset:192
	v_mul_f32_e32 v4, v11, v98
	v_mul_f32_e32 v4, v4, v6
	v_cvt_pk_bf16_f32 v7, v4, v147
	v_lshl_add_u64 v[4:5], v[2:3], 0, v[70:71]
	ds_write_b16 v162, v7 offset:2240
	v_mul_f32_e32 v4, v13, v101
	v_mul_f32_e32 v4, v4, v6
	v_cvt_pk_bf16_f32 v7, v4, v147
	v_lshl_add_u64 v[4:5], v[2:3], 0, v[72:73]
	ds_write_b16 v162, v7 offset:4288
	v_mul_f32_e32 v4, v19, v100
	v_mul_f32_e32 v4, v4, v6
	v_cvt_pk_bf16_f32 v7, v4, v147
	v_lshl_add_u64 v[4:5], v[2:3], 0, v[74:75]
	ds_write_b16 v162, v7 offset:6336
	v_mul_f32_e32 v4, v25, v103
	v_mul_f32_e32 v4, v4, v6
	v_cvt_pk_bf16_f32 v7, v4, v147
	v_lshl_add_u64 v[4:5], v[2:3], 0, v[76:77]
	ds_write_b16 v162, v7 offset:16576
	v_mul_f32_e32 v4, v29, v102
	v_mul_f32_e32 v4, v4, v6
	v_cvt_pk_bf16_f32 v7, v4, v147
	v_lshl_add_u64 v[4:5], v[2:3], 0, v[78:79]
	ds_write_b16 v162, v7 offset:18624
	v_mul_f32_e32 v4, v35, v105
	v_mul_f32_e32 v4, v4, v6
	v_cvt_pk_bf16_f32 v7, v4, v147
	v_lshl_add_u64 v[4:5], v[2:3], 0, v[80:81]
	ds_write_b16 v162, v7 offset:20672
	v_mul_f32_e32 v4, v39, v104
	v_mul_f32_e32 v4, v4, v6
	v_cvt_pk_bf16_f32 v7, v4, v147
	v_lshl_add_u64 v[4:5], v[2:3], 0, v[82:83]
	ds_write_b16 v162, v7 offset:22720
	v_mul_f32_e32 v4, v47, v108
	v_mul_f32_e32 v4, v4, v6
	v_cvt_pk_bf16_f32 v7, v4, v147
	v_lshl_add_u64 v[4:5], v[2:3], 0, v[84:85]
	ds_write_b16 v162, v7 offset:32960
	v_mul_f32_e32 v4, v51, v107
	v_mul_f32_e32 v4, v4, v6
	v_cvt_pk_bf16_f32 v7, v4, v147
	v_lshl_add_u64 v[4:5], v[2:3], 0, v[86:87]
	ds_write_b16 v162, v7 offset:35008
	v_mul_f32_e32 v4, v55, v113
	v_mul_f32_e32 v4, v4, v6
	v_cvt_pk_bf16_f32 v7, v4, v147
	v_lshl_add_u64 v[4:5], v[2:3], 0, v[88:89]
	ds_write_b16 v162, v7 offset:37056
	v_mul_f32_e32 v4, v57, v114
	v_mul_f32_e32 v4, v4, v6
	v_cvt_pk_bf16_f32 v7, v4, v147
	v_lshl_add_u64 v[4:5], v[2:3], 0, v[90:91]
	ds_write_b16 v162, v7 offset:39104
	v_mul_f32_e32 v4, v59, v115
	v_mul_f32_e32 v4, v4, v6
	v_cvt_pk_bf16_f32 v7, v4, v147
	v_lshl_add_u64 v[4:5], v[2:3], 0, v[92:93]
	ds_write_b16 v162, v7 offset:49344
	v_mul_f32_e32 v4, v61, v116
	v_mul_f32_e32 v4, v4, v6
	v_cvt_pk_bf16_f32 v7, v4, v147
	v_lshl_add_u64 v[4:5], v[2:3], 0, v[94:95]
	ds_write_b16 v162, v7 offset:51392
	v_mul_f32_e32 v4, v63, v117
	v_mul_f32_e32 v4, v4, v6
	v_cvt_pk_bf16_f32 v7, v4, v147
	v_lshl_add_u64 v[4:5], v[2:3], 0, v[96:97]
	ds_write_b16 v162, v7 offset:53440
	v_mul_f32_e32 v4, v65, v118
	v_mul_f32_e32 v4, v4, v6
	v_lshl_add_u64 v[2:3], v[2:3], 0, v[146:147]
	v_cvt_pk_bf16_f32 v4, v4, v147
	ds_write_b16 v162, v4 offset:55488
	s_waitcnt lgkmcnt(0)
	v_and_b32_e32 v163, 63, v0
	v_lshrrev_b32_e32 v166, 4, v163
	v_and_b32_e32 v163, 15, v163
	v_lshlrev_b32_e32 v164, 4, v163
	v_mov_b32_e32 v165, 0
	v_lshrrev_b32_e32 v167, 6, v0
	v_lshl_add_u32 v163, v167, 8, v164
	v_lshl_add_u32 v163, v166, 11, v163
	v_add_u32_e32 v163, 0x12800, v163
	ds_read_b128 v[120:123], v163
	ds_read_b128 v[124:127], v163 offset:8192
	ds_read_b128 v[128:131], v163 offset:16384
	ds_read_b128 v[132:135], v163 offset:24576
	ds_read_b128 v[136:139], v163 offset:32768
	ds_read_b128 v[140:143], v163 offset:40960
	ds_read_b128 v[148:151], v163 offset:49152
	ds_read_b128 v[152:155], v163 offset:57344
	v_lshl_add_u32 v167, v167, 5, v166
	v_add_u32_e32 v167, s30, v167
	v_lshlrev_b32_e32 v156, 13, v167
	v_mov_b32_e32 v157, 0
	v_lshl_add_u64 v[156:157], s[48:49], 0, v[156:157]
	v_lshl_add_u64 v[156:157], v[156:157], 0, s[76:77]
	v_lshl_add_u64 v[156:157], v[156:157], 0, v[164:165]
	v_mov_b32_e32 v160, 0x8000
	v_mov_b32_e32 v161, 0
	v_lshl_add_u64 v[158:159], v[156:157], 0, v[160:161]
	s_waitcnt lgkmcnt(7)
	global_store_dwordx4 v[156:157], v[120:123], off
	s_waitcnt lgkmcnt(6)
	global_store_dwordx4 v[158:159], v[124:127], off
	v_lshl_add_u64 v[156:157], v[158:159], 0, v[160:161]
	s_waitcnt lgkmcnt(5)
	global_store_dwordx4 v[156:157], v[128:131], off
	v_lshl_add_u64 v[158:159], v[156:157], 0, v[160:161]
	s_waitcnt lgkmcnt(4)
	global_store_dwordx4 v[158:159], v[132:135], off
	v_lshl_add_u64 v[156:157], v[158:159], 0, v[160:161]
	s_waitcnt lgkmcnt(3)
	global_store_dwordx4 v[156:157], v[136:139], off
	v_lshl_add_u64 v[158:159], v[156:157], 0, v[160:161]
	s_waitcnt lgkmcnt(2)
	global_store_dwordx4 v[158:159], v[140:143], off
	v_lshl_add_u64 v[156:157], v[158:159], 0, v[160:161]
	s_waitcnt lgkmcnt(1)
	global_store_dwordx4 v[156:157], v[148:151], off
	v_lshl_add_u64 v[158:159], v[156:157], 0, v[160:161]
	s_waitcnt lgkmcnt(0)
	global_store_dwordx4 v[158:159], v[152:155], off
	s_nop 1
	s_cbranch_scc0 .LBB0_455
